# own step 0: per-tile counted LDS waits for the four bias-init fragments instead of one wait for all; b2 scalar load issued after them
# speedup vs baseline: 1.0059x; 1.0006x over previous
.LBB1_4:
	s_and_saveexec_b64 s[8:9], s[2:3]
	v_perm_b32 v5, v1, v102, s23
	v_perm_b32 v9, v121, v103, s23
	s_or_b64 exec, exec, s[8:9]
	v_mov_b32_e32 v144, v1
	v_mov_b32_e32 v145, v121
	v_mfma_f32_16x16x32_f16 v[164:167], v[30:33], v[2:5], 0
	v_mfma_f32_16x16x32_f16 v[180:183], v[22:25], v[2:5], 0
	s_cmp_lg_u32 s22, 0x818000
	v_permlane32_swap_b32_e32 v1, v144
	v_permlane32_swap_b32_e32 v121, v145
	v_mfma_f32_16x16x32_f16 v[168:171], v[30:33], v[6:9], 0
	v_mfma_f32_16x16x32_f16 v[184:187], v[22:25], v[6:9], 0
	s_cselect_b32 s9, s11, 15
	s_and_saveexec_b64 s[32:33], s[2:3]
	v_perm_b32 v17, v144, v115, s23
	v_perm_b32 v29, v145, v116, s23
	s_or_b64 exec, exec, s[32:33]
	v_mfma_f32_16x16x32_f16 v[172:175], v[30:33], v[14:17], 0
	v_mfma_f32_16x16x32_f16 v[188:191], v[22:25], v[14:17], 0
	v_mfma_f32_16x16x32_f16 v[176:179], v[30:33], v[26:29], 0
	v_mfma_f32_16x16x32_f16 v[192:195], v[22:25], v[26:29], 0
	v_mfma_f32_16x16x32_f16 v[208:211], v[18:21], v[2:5], 0
	v_mfma_f32_16x16x32_f16 v[224:227], v[10:13], v[2:5], 0
	v_cvt_pk_f16_f32 v122, v164, v165
	v_cvt_pk_f16_f32 v123, v166, v167
	v_pk_max_f16 v122, v122, 0
	v_pk_max_f16 v123, v123, 0
	v_cvt_pk_f16_f32 v124, v180, v181
	v_cvt_pk_f16_f32 v125, v182, v183
	v_pk_max_f16 v124, v124, 0
	v_pk_max_f16 v125, v125, 0
	ds_write_b128 v107, v[122:125]
	v_mfma_f32_16x16x32_f16 v[212:215], v[18:21], v[6:9], 0
	v_mfma_f32_16x16x32_f16 v[228:231], v[10:13], v[6:9], 0
	v_cvt_pk_f16_f32 v126, v168, v169
	v_cvt_pk_f16_f32 v127, v170, v171
	v_pk_max_f16 v126, v126, 0
	v_pk_max_f16 v127, v127, 0
	v_cvt_pk_f16_f32 v128, v184, v185
	v_cvt_pk_f16_f32 v129, v186, v187
	v_pk_max_f16 v128, v128, 0
	v_pk_max_f16 v129, v129, 0
	ds_write_b128 v107, v[126:129] offset:16384
	v_mfma_f32_16x16x32_f16 v[216:219], v[18:21], v[14:17], 0
	v_mfma_f32_16x16x32_f16 v[232:235], v[10:13], v[14:17], 0
	v_cvt_pk_f16_f32 v134, v172, v173
	v_cvt_pk_f16_f32 v135, v174, v175
	v_pk_max_f16 v134, v134, 0
	v_pk_max_f16 v135, v135, 0
	v_cvt_pk_f16_f32 v136, v188, v189
	v_cvt_pk_f16_f32 v137, v190, v191
	v_pk_max_f16 v136, v136, 0
	v_pk_max_f16 v137, v137, 0
	ds_write_b128 v107, v[134:137] offset:32768
	v_mfma_f32_16x16x32_f16 v[220:223], v[18:21], v[26:29], 0
	v_mfma_f32_16x16x32_f16 v[236:239], v[10:13], v[26:29], 0
	v_cvt_pk_f16_f32 v138, v176, v177
	v_cvt_pk_f16_f32 v139, v178, v179
	v_pk_max_f16 v138, v138, 0
	v_pk_max_f16 v139, v139, 0
	v_cvt_pk_f16_f32 v140, v192, v193
	v_cvt_pk_f16_f32 v141, v194, v195
	v_pk_max_f16 v140, v140, 0
	v_pk_max_f16 v141, v141, 0
	ds_write_b128 v107, v[138:141] offset:49152
	v_add_u32_e32 v111, s64, v111
	v_add_u32_e32 v98, s65, v98
	s_lshl_b32 s20, s9, 7
	v_lshl_add_u64 v[0:1], s[20:21], 3, v[132:133]
	s_add_i32 s25, s22, s34
	s_lshl_b32 s8, s9, 8
	buffer_load_dwordx4 v[192:195], v147, s[16:19], s25 offen
	buffer_load_dwordx4 v[196:199], v148, s[16:19], s25 offen
	buffer_load_dwordx4 v[200:203], v149, s[16:19], s25 offen
	buffer_load_dwordx4 v[204:207], v150, s[16:19], s25 offen
	s_waitcnt vmcnt(19) lgkmcnt(8)
	v_mfma_f32_16x16x32_f16 v[164:167], v[58:61], v[122:125], v[240:243]
	v_cvt_pk_f16_f32 v142, v208, v209
	v_cvt_pk_f16_f32 v143, v210, v211
	v_mfma_f32_16x16x32_f16 v[168:171], v[58:61], v[126:129], v[240:243]
	v_pk_max_f16 v142, v142, 0
	v_pk_max_f16 v143, v143, 0
	v_mfma_f32_16x16x32_f16 v[172:175], v[58:61], v[134:137], v[240:243]
	v_cvt_pk_f16_f32 v144, v224, v225
	v_cvt_pk_f16_f32 v145, v226, v227
	v_mfma_f32_16x16x32_f16 v[10:13], v[58:61], v[138:141], v[240:243]
	v_pk_max_f16 v144, v144, 0
	v_pk_max_f16 v145, v145, 0
	ds_write_b128 v108, v[142:145]
	s_waitcnt vmcnt(18) lgkmcnt(8)
	v_mfma_f32_16x16x32_f16 v[58:61], v[54:57], v[122:125], v[244:247]
	v_cvt_pk_f16_f32 v152, v212, v213
	v_cvt_pk_f16_f32 v153, v214, v215
	v_mfma_f32_16x16x32_f16 v[176:179], v[54:57], v[126:129], v[244:247]
	v_pk_max_f16 v152, v152, 0
	v_pk_max_f16 v153, v153, 0
	v_mfma_f32_16x16x32_f16 v[180:183], v[54:57], v[134:137], v[244:247]
	v_cvt_pk_f16_f32 v154, v228, v229
	v_cvt_pk_f16_f32 v155, v230, v231
	v_mfma_f32_16x16x32_f16 v[18:21], v[54:57], v[138:141], v[244:247]
	v_pk_max_f16 v154, v154, 0
	v_pk_max_f16 v155, v155, 0
	ds_write_b128 v108, v[152:155] offset:16384
	s_waitcnt vmcnt(17) lgkmcnt(8)
	v_mfma_f32_16x16x32_f16 v[54:57], v[50:53], v[122:125], v[248:251]
	v_cvt_pk_f16_f32 v156, v216, v217
	v_cvt_pk_f16_f32 v157, v218, v219
	v_mfma_f32_16x16x32_f16 v[184:187], v[50:53], v[126:129], v[248:251]
	v_pk_max_f16 v156, v156, 0
	v_pk_max_f16 v157, v157, 0
	v_mfma_f32_16x16x32_f16 v[188:191], v[50:53], v[134:137], v[248:251]
	v_cvt_pk_f16_f32 v158, v232, v233
	v_cvt_pk_f16_f32 v159, v234, v235
	v_mfma_f32_16x16x32_f16 v[22:25], v[50:53], v[138:141], v[248:251]
	v_pk_max_f16 v158, v158, 0
	v_pk_max_f16 v159, v159, 0
	ds_write_b128 v108, v[156:159] offset:32768
	s_waitcnt vmcnt(16) lgkmcnt(8)
	v_mfma_f32_16x16x32_f16 v[50:53], v[38:41], v[122:125], v[252:255]
	s_load_dword s30, s[12:13], 0x0
	v_cvt_pk_f16_f32 v160, v220, v221
	v_cvt_pk_f16_f32 v161, v222, v223
	v_mfma_f32_16x16x32_f16 v[122:125], v[38:41], v[126:129], v[252:255]
	v_pk_max_f16 v160, v160, 0
	v_pk_max_f16 v161, v161, 0
	v_mfma_f32_16x16x32_f16 v[126:129], v[38:41], v[134:137], v[252:255]
	v_cvt_pk_f16_f32 v162, v236, v237
	v_cvt_pk_f16_f32 v163, v238, v239
	v_mfma_f32_16x16x32_f16 v[38:41], v[38:41], v[138:141], v[252:255]
	v_pk_max_f16 v162, v162, 0
	v_pk_max_f16 v163, v163, 0
	ds_write_b128 v108, v[160:163] offset:49152
	s_add_i32 s9, s22, s35
	s_waitcnt vmcnt(15)
	v_mfma_f32_16x16x32_f16 v[164:167], v[94:97], v[142:145], v[164:167]
	v_mfma_f32_16x16x32_f16 v[168:171], v[94:97], v[152:155], v[168:171]
	s_waitcnt vmcnt(14)
	v_mfma_f32_16x16x32_f16 v[58:61], v[90:93], v[142:145], v[58:61]
	v_mfma_f32_16x16x32_f16 v[176:179], v[90:93], v[152:155], v[176:179]
	s_waitcnt vmcnt(13)
	v_mfma_f32_16x16x32_f16 v[54:57], v[78:81], v[142:145], v[54:57]
	v_mfma_f32_16x16x32_f16 v[184:187], v[78:81], v[152:155], v[184:187]
	s_waitcnt vmcnt(12)
	v_mfma_f32_16x16x32_f16 v[50:53], v[34:37], v[142:145], v[50:53]
	buffer_load_dwordx4 v[140:143], v147, s[16:19], s9 offen
	buffer_load_dwordx4 v[220:223], v148, s[16:19], s9 offen
	v_mfma_f32_16x16x32_f16 v[122:125], v[34:37], v[152:155], v[122:125]
	buffer_load_dwordx4 v[152:155], v149, s[16:19], s9 offen
	buffer_load_dwordx4 v[224:227], v150, s[16:19], s9 offen
	s_mov_b32 s9, s21
	s_waitcnt lgkmcnt(0)
	s_barrier
	v_add_u32_e32 v99, s66, v99
	ds_read_b128 v[136:139], v99
	ds_read_b128 v[208:211], v99 offset:16384
	ds_read_b128 v[212:215], v99 offset:32768
	ds_read_b128 v[216:219], v99 offset:49152
	v_mfma_f32_16x16x32_f16 v[172:175], v[94:97], v[156:159], v[172:175]
	v_mfma_f32_16x16x32_f16 v[94:97], v[94:97], v[160:163], v[10:13]
	s_nop 2
	v_lshl_add_u64 v[10:11], s[8:9], 4, v[130:131]
	v_mfma_f32_16x16x32_f16 v[180:183], v[90:93], v[156:159], v[180:183]
	v_mfma_f32_16x16x32_f16 v[90:93], v[90:93], v[160:163], v[18:21]
	v_mfma_f32_16x16x32_f16 v[188:191], v[78:81], v[156:159], v[188:191]
	v_mfma_f32_16x16x32_f16 v[78:81], v[78:81], v[160:163], v[22:25]
	global_load_dwordx4 v[30:33], v[10:11], off
	s_nop 1
	global_load_dwordx4 v[22:25], v[10:11], off offset:1024
	global_load_dwordx4 v[18:21], v[10:11], off offset:2048
	s_nop 0
	global_load_dwordx4 v[10:13], v[10:11], off offset:3072
	s_nop 0
	global_load_dwordx2 v[134:135], v[0:1], off
	v_mfma_f32_16x16x32_f16 v[126:129], v[34:37], v[156:159], v[126:129]
	v_mfma_f32_16x16x32_f16 v[34:37], v[34:37], v[160:163], v[38:41]
	s_nop 2
	v_add_u32_e32 v100, s67, v100
	ds_read_b128 v[38:41], v100
	ds_read_b128 v[156:159], v100 offset:16384
	ds_read_b128 v[160:163], v100 offset:32768
	ds_read_b128 v[228:231], v100 offset:49152
	s_add_i32 s8, s22, s36
	s_waitcnt vmcnt(20) lgkmcnt(7)
	v_mfma_f32_16x16x32_f16 v[164:167], v[82:85], v[136:139], v[164:167]
	s_waitcnt lgkmcnt(6)
	v_mfma_f32_16x16x32_f16 v[168:171], v[82:85], v[208:211], v[168:171]
	s_waitcnt lgkmcnt(5)
	v_mfma_f32_16x16x32_f16 v[172:175], v[82:85], v[212:215], v[172:175]
	s_waitcnt lgkmcnt(4)
	v_mfma_f32_16x16x32_f16 v[82:85], v[82:85], v[216:219], v[94:97]
	s_waitcnt vmcnt(19)
	v_mfma_f32_16x16x32_f16 v[58:61], v[70:73], v[136:139], v[58:61]
	v_mfma_f32_16x16x32_f16 v[94:97], v[70:73], v[208:211], v[176:179]
	v_mfma_f32_16x16x32_f16 v[176:179], v[70:73], v[212:215], v[180:183]
	v_mfma_f32_16x16x32_f16 v[70:73], v[70:73], v[216:219], v[90:93]
	s_waitcnt vmcnt(18)
	v_mfma_f32_16x16x32_f16 v[54:57], v[62:65], v[136:139], v[54:57]
	v_mfma_f32_16x16x32_f16 v[90:93], v[62:65], v[208:211], v[184:187]
	v_mfma_f32_16x16x32_f16 v[180:183], v[62:65], v[212:215], v[188:191]
	v_mfma_f32_16x16x32_f16 v[62:65], v[62:65], v[216:219], v[78:81]
	s_waitcnt vmcnt(17)
	v_mfma_f32_16x16x32_f16 v[50:53], v[42:45], v[136:139], v[50:53]
	v_mfma_f32_16x16x32_f16 v[78:81], v[42:45], v[208:211], v[122:125]
	v_mfma_f32_16x16x32_f16 v[122:125], v[42:45], v[212:215], v[126:129]
	s_nop 2
	buffer_load_dwordx4 v[126:129], v147, s[16:19], s8 offen
	buffer_load_dwordx4 v[136:139], v148, s[16:19], s8 offen
	buffer_load_dwordx4 v[184:187], v149, s[16:19], s8 offen
	buffer_load_dwordx4 v[188:191], v150, s[16:19], s8 offen
	v_mfma_f32_16x16x32_f16 v[34:37], v[42:45], v[216:219], v[34:37]
	v_add_u32_e32 v111, s68, v111
	ds_read_b128 v[42:45], v111
	ds_read_b128 v[208:211], v111 offset:16384
	ds_read_b128 v[212:215], v111 offset:32768
	ds_read_b128 v[216:219], v111 offset:49152
	s_add_i32 s8, s22, s37
	s_waitcnt vmcnt(20) lgkmcnt(7)
	v_mfma_f32_16x16x32_f16 v[164:167], v[86:89], v[38:41], v[164:167]
	s_waitcnt lgkmcnt(6)
	v_mfma_f32_16x16x32_f16 v[168:171], v[86:89], v[156:159], v[168:171]
	s_waitcnt lgkmcnt(5)
	v_mfma_f32_16x16x32_f16 v[172:175], v[86:89], v[160:163], v[172:175]
	s_waitcnt lgkmcnt(4)
	v_mfma_f32_16x16x32_f16 v[82:85], v[86:89], v[228:231], v[82:85]
	s_waitcnt vmcnt(19)
	v_mfma_f32_16x16x32_f16 v[58:61], v[74:77], v[38:41], v[58:61]
	v_mfma_f32_16x16x32_f16 v[86:89], v[74:77], v[156:159], v[94:97]
	v_mfma_f32_16x16x32_f16 v[94:97], v[74:77], v[160:163], v[176:179]
	v_mfma_f32_16x16x32_f16 v[70:73], v[74:77], v[228:231], v[70:73]
	s_waitcnt vmcnt(18)
	v_mfma_f32_16x16x32_f16 v[54:57], v[66:69], v[38:41], v[54:57]
	v_mfma_f32_16x16x32_f16 v[74:77], v[66:69], v[156:159], v[90:93]
	v_mfma_f32_16x16x32_f16 v[90:93], v[66:69], v[160:163], v[180:183]
	v_mfma_f32_16x16x32_f16 v[62:65], v[66:69], v[228:231], v[62:65]
	s_waitcnt vmcnt(17)
	v_mfma_f32_16x16x32_f16 v[38:41], v[46:49], v[38:41], v[50:53]
	v_mfma_f32_16x16x32_f16 v[50:53], v[46:49], v[156:159], v[78:81]
	v_mfma_f32_16x16x32_f16 v[66:69], v[46:49], v[160:163], v[122:125]
	s_nop 1
	buffer_load_dwordx4 v[78:81], v147, s[16:19], s8 offen
	buffer_load_dwordx4 v[122:125], v148, s[16:19], s8 offen
	buffer_load_dwordx4 v[156:159], v149, s[16:19], s8 offen
	buffer_load_dwordx4 v[160:163], v150, s[16:19], s8 offen
	v_mfma_f32_16x16x32_f16 v[34:37], v[46:49], v[228:231], v[34:37]
	v_add_u32_e32 v98, s69, v98
	ds_read_b128 v[46:49], v98
	ds_read_b128 v[176:179], v98 offset:16384
	ds_read_b128 v[180:183], v98 offset:32768
	ds_read_b128 v[228:231], v98 offset:49152
	s_add_i32 s8, s22, s38
	s_waitcnt vmcnt(20) lgkmcnt(7)
	v_mfma_f32_16x16x32_f16 v[164:167], v[192:195], v[42:45], v[164:167]
	s_waitcnt lgkmcnt(6)
	v_mfma_f32_16x16x32_f16 v[168:171], v[192:195], v[208:211], v[168:171]
	s_waitcnt lgkmcnt(5)
	v_mfma_f32_16x16x32_f16 v[172:175], v[192:195], v[212:215], v[172:175]
	s_waitcnt lgkmcnt(4)
	v_mfma_f32_16x16x32_f16 v[82:85], v[192:195], v[216:219], v[82:85]
	s_waitcnt vmcnt(19)
	v_mfma_f32_16x16x32_f16 v[58:61], v[196:199], v[42:45], v[58:61]
	v_mfma_f32_16x16x32_f16 v[86:89], v[196:199], v[208:211], v[86:89]
	v_mfma_f32_16x16x32_f16 v[94:97], v[196:199], v[212:215], v[94:97]
	v_mfma_f32_16x16x32_f16 v[70:73], v[196:199], v[216:219], v[70:73]
	s_waitcnt vmcnt(18)
	v_mfma_f32_16x16x32_f16 v[54:57], v[200:203], v[42:45], v[54:57]
	v_mfma_f32_16x16x32_f16 v[74:77], v[200:203], v[208:211], v[74:77]
	v_mfma_f32_16x16x32_f16 v[90:93], v[200:203], v[212:215], v[90:93]
	v_mfma_f32_16x16x32_f16 v[62:65], v[200:203], v[216:219], v[62:65]
	s_waitcnt vmcnt(17)
	v_mfma_f32_16x16x32_f16 v[38:41], v[204:207], v[42:45], v[38:41]
	v_mfma_f32_16x16x32_f16 v[42:45], v[204:207], v[208:211], v[50:53]
	v_mfma_f32_16x16x32_f16 v[50:53], v[204:207], v[212:215], v[66:69]
	s_nop 2
	buffer_load_dwordx4 v[66:69], v147, s[16:19], s8 offen
	buffer_load_dwordx4 v[192:195], v148, s[16:19], s8 offen
	buffer_load_dwordx4 v[196:199], v149, s[16:19], s8 offen
	buffer_load_dwordx4 v[200:203], v150, s[16:19], s8 offen
	v_mfma_f32_16x16x32_f16 v[34:37], v[204:207], v[216:219], v[34:37]
	v_add_u32_e32 v99, s70, v99
	ds_read_b128 v[204:207], v99
	ds_read_b128 v[208:211], v99 offset:16384
	ds_read_b128 v[212:215], v99 offset:32768
	ds_read_b128 v[216:219], v99 offset:49152
	s_add_i32 s8, s22, s39
	s_waitcnt vmcnt(20) lgkmcnt(7)
	v_mfma_f32_16x16x32_f16 v[164:167], v[140:143], v[46:49], v[164:167]
	s_waitcnt lgkmcnt(6)
	v_mfma_f32_16x16x32_f16 v[168:171], v[140:143], v[176:179], v[168:171]
	s_waitcnt lgkmcnt(5)
	v_mfma_f32_16x16x32_f16 v[172:175], v[140:143], v[180:183], v[172:175]
	s_waitcnt lgkmcnt(4)
	v_mfma_f32_16x16x32_f16 v[82:85], v[140:143], v[228:231], v[82:85]
	s_waitcnt vmcnt(19)
	v_mfma_f32_16x16x32_f16 v[58:61], v[220:223], v[46:49], v[58:61]
	v_mfma_f32_16x16x32_f16 v[86:89], v[220:223], v[176:179], v[86:89]
	s_waitcnt vmcnt(18)
	v_mfma_f32_16x16x32_f16 v[54:57], v[152:155], v[46:49], v[54:57]
	v_mfma_f32_16x16x32_f16 v[74:77], v[152:155], v[176:179], v[74:77]
	v_mfma_f32_16x16x32_f16 v[90:93], v[152:155], v[180:183], v[90:93]
	v_mfma_f32_16x16x32_f16 v[62:65], v[152:155], v[228:231], v[62:65]
	s_waitcnt vmcnt(17)
	v_mfma_f32_16x16x32_f16 v[38:41], v[224:227], v[46:49], v[38:41]
	v_mfma_f32_16x16x32_f16 v[42:45], v[224:227], v[176:179], v[42:45]
	v_mfma_f32_16x16x32_f16 v[46:49], v[224:227], v[180:183], v[50:53]
	s_nop 2
	buffer_load_dwordx4 v[50:53], v147, s[16:19], s8 offen
	buffer_load_dwordx4 v[140:143], v148, s[16:19], s8 offen
	buffer_load_dwordx4 v[152:155], v149, s[16:19], s8 offen
	buffer_load_dwordx4 v[176:179], v150, s[16:19], s8 offen
	v_mfma_f32_16x16x32_f16 v[94:97], v[220:223], v[180:183], v[94:97]
	v_mfma_f32_16x16x32_f16 v[70:73], v[220:223], v[228:231], v[70:73]
	v_mfma_f32_16x16x32_f16 v[34:37], v[224:227], v[228:231], v[34:37]
	v_add_u32_e32 v100, s71, v100
	ds_read_b128 v[180:183], v100
	ds_read_b128 v[220:223], v100 offset:16384
	ds_read_b128 v[224:227], v100 offset:32768
	ds_read_b128 v[228:231], v100 offset:49152
	s_add_i32 s8, s22, s40
	s_waitcnt vmcnt(15) lgkmcnt(7)
	v_mfma_f32_16x16x32_f16 v[164:167], v[126:129], v[204:207], v[164:167]
	s_waitcnt lgkmcnt(6)
	v_mfma_f32_16x16x32_f16 v[168:171], v[126:129], v[208:211], v[168:171]
	s_waitcnt lgkmcnt(5)
	v_mfma_f32_16x16x32_f16 v[172:175], v[126:129], v[212:215], v[172:175]
	s_waitcnt lgkmcnt(4)
	v_mfma_f32_16x16x32_f16 v[82:85], v[126:129], v[216:219], v[82:85]
	s_waitcnt vmcnt(14)
	v_mfma_f32_16x16x32_f16 v[58:61], v[136:139], v[204:207], v[58:61]
	v_mfma_f32_16x16x32_f16 v[86:89], v[136:139], v[208:211], v[86:89]
	v_mfma_f32_16x16x32_f16 v[94:97], v[136:139], v[212:215], v[94:97]
	v_mfma_f32_16x16x32_f16 v[70:73], v[136:139], v[216:219], v[70:73]
	s_waitcnt vmcnt(13)
	v_mfma_f32_16x16x32_f16 v[54:57], v[184:187], v[204:207], v[54:57]
	v_mfma_f32_16x16x32_f16 v[74:77], v[184:187], v[208:211], v[74:77]
	v_mfma_f32_16x16x32_f16 v[90:93], v[184:187], v[212:215], v[90:93]
	v_mfma_f32_16x16x32_f16 v[62:65], v[184:187], v[216:219], v[62:65]
	s_waitcnt vmcnt(12)
	v_mfma_f32_16x16x32_f16 v[38:41], v[188:191], v[204:207], v[38:41]
	buffer_load_dwordx4 v[126:129], v147, s[16:19], s8 offen
	buffer_load_dwordx4 v[136:139], v148, s[16:19], s8 offen
	buffer_load_dwordx4 v[184:187], v149, s[16:19], s8 offen
	buffer_load_dwordx4 v[204:207], v150, s[16:19], s8 offen
	v_mfma_f32_16x16x32_f16 v[42:45], v[188:191], v[208:211], v[42:45]
	v_mfma_f32_16x16x32_f16 v[46:49], v[188:191], v[212:215], v[46:49]
	v_mfma_f32_16x16x32_f16 v[34:37], v[188:191], v[216:219], v[34:37]
	v_add_u32_e32 v111, s72, v111
	ds_read_b128 v[188:191], v111
	ds_read_b128 v[208:211], v111 offset:16384
	ds_read_b128 v[212:215], v111 offset:32768
	ds_read_b128 v[216:219], v111 offset:49152
	s_add_i32 s8, s22, s41
	s_waitcnt vmcnt(15) lgkmcnt(7)
	v_mfma_f32_16x16x32_f16 v[164:167], v[78:81], v[180:183], v[164:167]
	s_waitcnt lgkmcnt(6)
	v_mfma_f32_16x16x32_f16 v[168:171], v[78:81], v[220:223], v[168:171]
	s_waitcnt lgkmcnt(5)
	v_mfma_f32_16x16x32_f16 v[172:175], v[78:81], v[224:227], v[172:175]
	s_waitcnt lgkmcnt(4)
	v_mfma_f32_16x16x32_f16 v[78:81], v[78:81], v[228:231], v[82:85]
	s_waitcnt vmcnt(14)
	v_mfma_f32_16x16x32_f16 v[58:61], v[122:125], v[180:183], v[58:61]
	v_mfma_f32_16x16x32_f16 v[82:85], v[122:125], v[220:223], v[86:89]
	v_mfma_f32_16x16x32_f16 v[86:89], v[122:125], v[224:227], v[94:97]
	v_mfma_f32_16x16x32_f16 v[70:73], v[122:125], v[228:231], v[70:73]
	s_waitcnt vmcnt(13)
	v_mfma_f32_16x16x32_f16 v[54:57], v[156:159], v[180:183], v[54:57]
	v_mfma_f32_16x16x32_f16 v[74:77], v[156:159], v[220:223], v[74:77]
	v_mfma_f32_16x16x32_f16 v[90:93], v[156:159], v[224:227], v[90:93]
	v_mfma_f32_16x16x32_f16 v[62:65], v[156:159], v[228:231], v[62:65]
	s_waitcnt vmcnt(12)
	v_mfma_f32_16x16x32_f16 v[38:41], v[160:163], v[180:183], v[38:41]
	buffer_load_dwordx4 v[94:97], v147, s[16:19], s8 offen
	buffer_load_dwordx4 v[122:125], v148, s[16:19], s8 offen
	buffer_load_dwordx4 v[156:159], v149, s[16:19], s8 offen
	buffer_load_dwordx4 v[180:183], v150, s[16:19], s8 offen
	v_mfma_f32_16x16x32_f16 v[42:45], v[160:163], v[220:223], v[42:45]
	v_mfma_f32_16x16x32_f16 v[46:49], v[160:163], v[224:227], v[46:49]
	v_mfma_f32_16x16x32_f16 v[34:37], v[160:163], v[228:231], v[34:37]
	v_add_u32_e32 v98, s73, v98
	ds_read_b128 v[160:163], v98
	ds_read_b128 v[220:223], v98 offset:16384
	ds_read_b128 v[224:227], v98 offset:32768
	ds_read_b128 v[228:231], v98 offset:49152
	s_add_i32 s8, s22, s42
	s_waitcnt vmcnt(15) lgkmcnt(7)
	v_mfma_f32_16x16x32_f16 v[164:167], v[66:69], v[188:191], v[164:167]
	s_waitcnt lgkmcnt(6)
	v_mfma_f32_16x16x32_f16 v[168:171], v[66:69], v[208:211], v[168:171]
	s_waitcnt lgkmcnt(5)
	v_mfma_f32_16x16x32_f16 v[172:175], v[66:69], v[212:215], v[172:175]
	s_waitcnt lgkmcnt(4)
	v_mfma_f32_16x16x32_f16 v[66:69], v[66:69], v[216:219], v[78:81]
	s_waitcnt vmcnt(14)
	v_mfma_f32_16x16x32_f16 v[58:61], v[192:195], v[188:191], v[58:61]
	v_mfma_f32_16x16x32_f16 v[78:81], v[192:195], v[208:211], v[82:85]
	v_mfma_f32_16x16x32_f16 v[82:85], v[192:195], v[212:215], v[86:89]
	v_mfma_f32_16x16x32_f16 v[70:73], v[192:195], v[216:219], v[70:73]
	s_waitcnt vmcnt(13)
	v_mfma_f32_16x16x32_f16 v[54:57], v[196:199], v[188:191], v[54:57]
	v_mfma_f32_16x16x32_f16 v[74:77], v[196:199], v[208:211], v[74:77]
	v_mfma_f32_16x16x32_f16 v[86:89], v[196:199], v[212:215], v[90:93]
	v_mfma_f32_16x16x32_f16 v[62:65], v[196:199], v[216:219], v[62:65]
	s_waitcnt vmcnt(12)
	v_mfma_f32_16x16x32_f16 v[38:41], v[200:203], v[188:191], v[38:41]
	buffer_load_dwordx4 v[90:93], v147, s[16:19], s8 offen
	buffer_load_dwordx4 v[188:191], v148, s[16:19], s8 offen
	buffer_load_dwordx4 v[192:195], v149, s[16:19], s8 offen
	buffer_load_dwordx4 v[196:199], v150, s[16:19], s8 offen
	v_mfma_f32_16x16x32_f16 v[42:45], v[200:203], v[208:211], v[42:45]
	v_mfma_f32_16x16x32_f16 v[46:49], v[200:203], v[212:215], v[46:49]
	v_mfma_f32_16x16x32_f16 v[34:37], v[200:203], v[216:219], v[34:37]
	v_add_u32_e32 v99, s74, v99
	ds_read_b128 v[200:203], v99
	ds_read_b128 v[208:211], v99 offset:16384
	ds_read_b128 v[212:215], v99 offset:32768
	ds_read_b128 v[216:219], v99 offset:49152
	s_add_i32 s8, s22, s43
	s_waitcnt vmcnt(15) lgkmcnt(7)
	v_mfma_f32_16x16x32_f16 v[164:167], v[50:53], v[160:163], v[164:167]
	s_waitcnt lgkmcnt(6)
	v_mfma_f32_16x16x32_f16 v[168:171], v[50:53], v[220:223], v[168:171]
	s_waitcnt lgkmcnt(5)
	v_mfma_f32_16x16x32_f16 v[172:175], v[50:53], v[224:227], v[172:175]
	s_waitcnt lgkmcnt(4)
	v_mfma_f32_16x16x32_f16 v[50:53], v[50:53], v[228:231], v[66:69]
	s_waitcnt vmcnt(14)
	v_mfma_f32_16x16x32_f16 v[58:61], v[140:143], v[160:163], v[58:61]
	v_mfma_f32_16x16x32_f16 v[66:69], v[140:143], v[220:223], v[78:81]
	v_mfma_f32_16x16x32_f16 v[78:81], v[140:143], v[224:227], v[82:85]
	v_mfma_f32_16x16x32_f16 v[70:73], v[140:143], v[228:231], v[70:73]
	s_waitcnt vmcnt(13)
	v_mfma_f32_16x16x32_f16 v[54:57], v[152:155], v[160:163], v[54:57]
	v_mfma_f32_16x16x32_f16 v[74:77], v[152:155], v[220:223], v[74:77]
	v_mfma_f32_16x16x32_f16 v[82:85], v[152:155], v[224:227], v[86:89]
	v_mfma_f32_16x16x32_f16 v[62:65], v[152:155], v[228:231], v[62:65]
	s_waitcnt vmcnt(12)
	v_mfma_f32_16x16x32_f16 v[38:41], v[176:179], v[160:163], v[38:41]
	buffer_load_dwordx4 v[86:89], v147, s[16:19], s8 offen
	buffer_load_dwordx4 v[140:143], v148, s[16:19], s8 offen
	buffer_load_dwordx4 v[152:155], v149, s[16:19], s8 offen
	buffer_load_dwordx4 v[160:163], v150, s[16:19], s8 offen
	v_mfma_f32_16x16x32_f16 v[42:45], v[176:179], v[220:223], v[42:45]
	v_mfma_f32_16x16x32_f16 v[46:49], v[176:179], v[224:227], v[46:49]
	v_mfma_f32_16x16x32_f16 v[34:37], v[176:179], v[228:231], v[34:37]
	v_add_u32_e32 v100, s75, v100
	ds_read_b128 v[176:179], v100
	ds_read_b128 v[220:223], v100 offset:16384
	ds_read_b128 v[224:227], v100 offset:32768
	ds_read_b128 v[228:231], v100 offset:49152
	s_add_i32 s8, s22, s44
	s_waitcnt vmcnt(15) lgkmcnt(7)
	v_mfma_f32_16x16x32_f16 v[164:167], v[126:129], v[200:203], v[164:167]
	s_waitcnt lgkmcnt(6)
	v_mfma_f32_16x16x32_f16 v[168:171], v[126:129], v[208:211], v[168:171]
	s_waitcnt lgkmcnt(5)
	v_mfma_f32_16x16x32_f16 v[172:175], v[126:129], v[212:215], v[172:175]
	s_waitcnt lgkmcnt(4)
	v_mfma_f32_16x16x32_f16 v[50:53], v[126:129], v[216:219], v[50:53]
	s_waitcnt vmcnt(14)
	v_mfma_f32_16x16x32_f16 v[58:61], v[136:139], v[200:203], v[58:61]
	v_mfma_f32_16x16x32_f16 v[66:69], v[136:139], v[208:211], v[66:69]
	v_mfma_f32_16x16x32_f16 v[78:81], v[136:139], v[212:215], v[78:81]
	v_mfma_f32_16x16x32_f16 v[70:73], v[136:139], v[216:219], v[70:73]
	s_waitcnt vmcnt(13)
	v_mfma_f32_16x16x32_f16 v[54:57], v[184:187], v[200:203], v[54:57]
	v_mfma_f32_16x16x32_f16 v[74:77], v[184:187], v[208:211], v[74:77]
	v_mfma_f32_16x16x32_f16 v[82:85], v[184:187], v[212:215], v[82:85]
	v_mfma_f32_16x16x32_f16 v[62:65], v[184:187], v[216:219], v[62:65]
	s_waitcnt vmcnt(12)
	v_mfma_f32_16x16x32_f16 v[38:41], v[204:207], v[200:203], v[38:41]
	buffer_load_dwordx4 v[126:129], v147, s[16:19], s8 offen
	buffer_load_dwordx4 v[136:139], v148, s[16:19], s8 offen
	buffer_load_dwordx4 v[184:187], v149, s[16:19], s8 offen
	buffer_load_dwordx4 v[200:203], v150, s[16:19], s8 offen
	v_mfma_f32_16x16x32_f16 v[42:45], v[204:207], v[208:211], v[42:45]
	v_mfma_f32_16x16x32_f16 v[46:49], v[204:207], v[212:215], v[46:49]
	v_mfma_f32_16x16x32_f16 v[34:37], v[204:207], v[216:219], v[34:37]
	v_add_u32_e32 v111, s76, v111
	ds_read_b128 v[204:207], v111
	ds_read_b128 v[208:211], v111 offset:16384
	ds_read_b128 v[212:215], v111 offset:32768
	ds_read_b128 v[216:219], v111 offset:49152
	s_add_i32 s8, s22, s45
	s_waitcnt vmcnt(15) lgkmcnt(7)
	v_mfma_f32_16x16x32_f16 v[164:167], v[94:97], v[176:179], v[164:167]
	s_waitcnt lgkmcnt(6)
	v_mfma_f32_16x16x32_f16 v[168:171], v[94:97], v[220:223], v[168:171]
	s_waitcnt vmcnt(14)
	v_mfma_f32_16x16x32_f16 v[58:61], v[122:125], v[176:179], v[58:61]
	v_mfma_f32_16x16x32_f16 v[66:69], v[122:125], v[220:223], v[66:69]
	s_waitcnt lgkmcnt(5)
	v_mfma_f32_16x16x32_f16 v[78:81], v[122:125], v[224:227], v[78:81]
	s_waitcnt lgkmcnt(4)
	v_mfma_f32_16x16x32_f16 v[70:73], v[122:125], v[228:231], v[70:73]
	s_waitcnt vmcnt(13)
	v_mfma_f32_16x16x32_f16 v[54:57], v[156:159], v[176:179], v[54:57]
	v_mfma_f32_16x16x32_f16 v[74:77], v[156:159], v[220:223], v[74:77]
	v_mfma_f32_16x16x32_f16 v[82:85], v[156:159], v[224:227], v[82:85]
	v_mfma_f32_16x16x32_f16 v[62:65], v[156:159], v[228:231], v[62:65]
	s_waitcnt vmcnt(12)
	v_mfma_f32_16x16x32_f16 v[38:41], v[180:183], v[176:179], v[38:41]
	v_mfma_f32_16x16x32_f16 v[42:45], v[180:183], v[220:223], v[42:45]
	buffer_load_dwordx4 v[122:125], v147, s[16:19], s8 offen
	buffer_load_dwordx4 v[156:159], v148, s[16:19], s8 offen
	buffer_load_dwordx4 v[176:179], v149, s[16:19], s8 offen
	buffer_load_dwordx4 v[220:223], v150, s[16:19], s8 offen
	v_mfma_f32_16x16x32_f16 v[50:53], v[94:97], v[228:231], v[50:53]
	v_mfma_f32_16x16x32_f16 v[46:49], v[180:183], v[224:227], v[46:49]
	v_mfma_f32_16x16x32_f16 v[34:37], v[180:183], v[228:231], v[34:37]
	v_mfma_f32_16x16x32_f16 v[172:175], v[94:97], v[224:227], v[172:175]
	v_add_u32_e32 v98, s77, v98
	ds_read_b128 v[94:97], v98
	ds_read_b128 v[180:183], v98 offset:16384
	ds_read_b128 v[224:227], v98 offset:32768
	ds_read_b128 v[228:231], v98 offset:49152
	s_add_i32 s8, s22, s46
	s_waitcnt vmcnt(15) lgkmcnt(7)
	v_mfma_f32_16x16x32_f16 v[164:167], v[90:93], v[204:207], v[164:167]
	s_waitcnt lgkmcnt(6)
	v_mfma_f32_16x16x32_f16 v[168:171], v[90:93], v[208:211], v[168:171]
	s_waitcnt lgkmcnt(5)
	v_mfma_f32_16x16x32_f16 v[172:175], v[90:93], v[212:215], v[172:175]
	s_waitcnt lgkmcnt(4)
	v_mfma_f32_16x16x32_f16 v[90:93], v[90:93], v[216:219], v[50:53]
	s_waitcnt vmcnt(14)
	v_mfma_f32_16x16x32_f16 v[232:235], v[188:191], v[204:207], v[58:61]
	v_mfma_f32_16x16x32_f16 v[66:69], v[188:191], v[208:211], v[66:69]
	v_mfma_f32_16x16x32_f16 v[78:81], v[188:191], v[212:215], v[78:81]
	v_mfma_f32_16x16x32_f16 v[70:73], v[188:191], v[216:219], v[70:73]
	s_waitcnt vmcnt(13)
	v_mfma_f32_16x16x32_f16 v[188:191], v[192:195], v[204:207], v[54:57]
	v_mfma_f32_16x16x32_f16 v[74:77], v[192:195], v[208:211], v[74:77]
	v_mfma_f32_16x16x32_f16 v[82:85], v[192:195], v[212:215], v[82:85]
	v_mfma_f32_16x16x32_f16 v[62:65], v[192:195], v[216:219], v[62:65]
	s_waitcnt vmcnt(12)
	v_mfma_f32_16x16x32_f16 v[192:195], v[196:199], v[204:207], v[38:41]
	buffer_load_dwordx4 v[58:61], v147, s[16:19], s8 offen
	buffer_load_dwordx4 v[54:57], v148, s[16:19], s8 offen
	buffer_load_dwordx4 v[50:53], v149, s[16:19], s8 offen
	buffer_load_dwordx4 v[38:41], v150, s[16:19], s8 offen
	v_mfma_f32_16x16x32_f16 v[42:45], v[196:199], v[208:211], v[42:45]
	v_mfma_f32_16x16x32_f16 v[46:49], v[196:199], v[212:215], v[46:49]
	v_mfma_f32_16x16x32_f16 v[196:199], v[196:199], v[216:219], v[34:37]
	v_add_u32_e32 v99, s78, v99
	ds_read_b128 v[204:207], v99
	ds_read_b128 v[208:211], v99 offset:16384
	ds_read_b128 v[212:215], v99 offset:32768
	ds_read_b128 v[216:219], v99 offset:49152
	s_add_i32 s8, s22, s47
	s_waitcnt vmcnt(15) lgkmcnt(7)
	v_mfma_f32_16x16x32_f16 v[164:167], v[86:89], v[94:97], v[164:167]
	s_waitcnt lgkmcnt(6)
	v_mfma_f32_16x16x32_f16 v[168:171], v[86:89], v[180:183], v[168:171]
	s_waitcnt lgkmcnt(5)
	v_mfma_f32_16x16x32_f16 v[172:175], v[86:89], v[224:227], v[172:175]
	s_waitcnt lgkmcnt(4)
	v_mfma_f32_16x16x32_f16 v[86:89], v[86:89], v[228:231], v[90:93]
	s_waitcnt vmcnt(14)
	v_mfma_f32_16x16x32_f16 v[232:235], v[140:143], v[94:97], v[232:235]
	v_mfma_f32_16x16x32_f16 v[66:69], v[140:143], v[180:183], v[66:69]
	v_mfma_f32_16x16x32_f16 v[236:239], v[140:143], v[224:227], v[78:81]
	v_mfma_f32_16x16x32_f16 v[70:73], v[140:143], v[228:231], v[70:73]
	s_waitcnt vmcnt(13)
	v_mfma_f32_16x16x32_f16 v[140:143], v[152:155], v[94:97], v[188:191]
	v_mfma_f32_16x16x32_f16 v[74:77], v[152:155], v[180:183], v[74:77]
	v_mfma_f32_16x16x32_f16 v[82:85], v[152:155], v[224:227], v[82:85]
	v_mfma_f32_16x16x32_f16 v[62:65], v[152:155], v[228:231], v[62:65]
	s_waitcnt vmcnt(12)
	v_mfma_f32_16x16x32_f16 v[152:155], v[160:163], v[94:97], v[192:195]
	buffer_load_dwordx4 v[94:97], v147, s[16:19], s8 offen
	buffer_load_dwordx4 v[90:93], v148, s[16:19], s8 offen
	buffer_load_dwordx4 v[78:81], v149, s[16:19], s8 offen
	buffer_load_dwordx4 v[34:37], v150, s[16:19], s8 offen
	v_mfma_f32_16x16x32_f16 v[42:45], v[160:163], v[180:183], v[42:45]
	v_mfma_f32_16x16x32_f16 v[46:49], v[160:163], v[224:227], v[46:49]
	v_mfma_f32_16x16x32_f16 v[160:163], v[160:163], v[228:231], v[196:199]
	v_add_u32_e32 v100, s79, v100
	ds_read_b128 v[180:183], v100
	ds_read_b128 v[188:191], v100 offset:16384
	ds_read_b128 v[192:195], v100 offset:32768
	ds_read_b128 v[196:199], v100 offset:49152
	s_add_i32 s8, s22, s48
	s_waitcnt vmcnt(15) lgkmcnt(7)
	v_mfma_f32_16x16x32_f16 v[164:167], v[126:129], v[204:207], v[164:167]
	s_waitcnt lgkmcnt(6)
	v_mfma_f32_16x16x32_f16 v[168:171], v[126:129], v[208:211], v[168:171]
	s_waitcnt lgkmcnt(5)
	v_mfma_f32_16x16x32_f16 v[172:175], v[126:129], v[212:215], v[172:175]
	s_waitcnt lgkmcnt(4)
	v_mfma_f32_16x16x32_f16 v[86:89], v[126:129], v[216:219], v[86:89]
	s_waitcnt vmcnt(14)
	v_mfma_f32_16x16x32_f16 v[126:129], v[136:139], v[204:207], v[232:235]
	v_mfma_f32_16x16x32_f16 v[66:69], v[136:139], v[208:211], v[66:69]
	v_mfma_f32_16x16x32_f16 v[224:227], v[136:139], v[212:215], v[236:239]
	v_mfma_f32_16x16x32_f16 v[136:139], v[136:139], v[216:219], v[70:73]
	s_waitcnt vmcnt(13)
	v_mfma_f32_16x16x32_f16 v[140:143], v[184:187], v[204:207], v[140:143]
	v_mfma_f32_16x16x32_f16 v[74:77], v[184:187], v[208:211], v[74:77]
	v_mfma_f32_16x16x32_f16 v[228:231], v[184:187], v[212:215], v[82:85]
	v_mfma_f32_16x16x32_f16 v[184:187], v[184:187], v[216:219], v[62:65]
	s_waitcnt vmcnt(12)
	v_mfma_f32_16x16x32_f16 v[152:155], v[200:203], v[204:207], v[152:155]
	v_mfma_f32_16x16x32_f16 v[204:207], v[200:203], v[208:211], v[42:45]
	buffer_load_dwordx4 v[82:85], v147, s[16:19], s8 offen
	buffer_load_dwordx4 v[70:73], v148, s[16:19], s8 offen
	buffer_load_dwordx4 v[62:65], v149, s[16:19], s8 offen
	buffer_load_dwordx4 v[42:45], v150, s[16:19], s8 offen
	v_mfma_f32_16x16x32_f16 v[46:49], v[200:203], v[212:215], v[46:49]
	v_mfma_f32_16x16x32_f16 v[160:163], v[200:203], v[216:219], v[160:163]
	v_add_u32_e32 v0, 0x1ac00, v104
	ds_read_b128 v[240:243], v0
	ds_read_b128 v[244:247], v0 offset:16
	s_waitcnt vmcnt(12) lgkmcnt(5)
	v_mfma_f32_16x16x32_f16 v[164:167], v[122:125], v[180:183], v[164:167]
	v_mfma_f32_16x16x32_f16 v[126:129], v[156:159], v[180:183], v[126:129]
	v_mfma_f32_16x16x32_f16 v[140:143], v[176:179], v[180:183], v[140:143]
	v_mfma_f32_16x16x32_f16 v[152:155], v[220:223], v[180:183], v[152:155]
	s_waitcnt lgkmcnt(4)
	v_mfma_f32_16x16x32_f16 v[168:171], v[122:125], v[188:191], v[168:171]
	v_mfma_f32_16x16x32_f16 v[208:211], v[156:159], v[188:191], v[66:69]
	v_mfma_f32_16x16x32_f16 v[212:215], v[176:179], v[188:191], v[74:77]
	v_mfma_f32_16x16x32_f16 v[204:207], v[220:223], v[188:191], v[204:207]
	s_waitcnt lgkmcnt(3)
	v_mfma_f32_16x16x32_f16 v[172:175], v[122:125], v[192:195], v[172:175]
	v_cvt_pk_f16_f32 v232, v164, v165
	v_cvt_pk_f16_f32 v233, v166, v167
	v_pk_max_f16 v232, v232, 0
	v_pk_max_f16 v233, v233, 0
	v_mfma_f32_16x16x32_f16 v[224:227], v[156:159], v[192:195], v[224:227]
	v_cvt_pk_f16_f32 v234, v126, v127
	v_cvt_pk_f16_f32 v235, v128, v129
	v_pk_max_f16 v234, v234, 0
	v_pk_max_f16 v235, v235, 0
	v_mfma_f32_16x16x32_f16 v[228:231], v[176:179], v[192:195], v[228:231]
	v_cvt_pk_f16_f32 v236, v140, v141
	v_cvt_pk_f16_f32 v237, v142, v143
	v_pk_max_f16 v236, v236, 0
	v_pk_max_f16 v237, v237, 0
	v_mfma_f32_16x16x32_f16 v[216:219], v[220:223], v[192:195], v[46:49]
	v_cvt_pk_f16_f32 v238, v152, v153
	v_cvt_pk_f16_f32 v239, v154, v155
	v_pk_max_f16 v238, v238, 0
	v_pk_max_f16 v239, v239, 0
	s_waitcnt lgkmcnt(2)
	v_mfma_f32_16x16x32_f16 v[200:203], v[122:125], v[196:199], v[86:89]
	v_cvt_pk_f16_f32 v180, v168, v169
	v_cvt_pk_f16_f32 v181, v170, v171
	v_pk_max_f16 v180, v180, 0
	v_pk_max_f16 v181, v181, 0
	s_add_i32 s8, s22, s49
	buffer_load_dwordx4 v[86:89], v147, s[16:19], s8 offen
	buffer_load_dwordx4 v[74:77], v148, s[16:19], s8 offen
	buffer_load_dwordx4 v[66:69], v149, s[16:19], s8 offen
	buffer_load_dwordx4 v[46:49], v150, s[16:19], s8 offen
	v_mfma_f32_16x16x32_f16 v[136:139], v[156:159], v[196:199], v[136:139]
	v_cvt_pk_f16_f32 v182, v208, v209
	v_cvt_pk_f16_f32 v183, v210, v211
	v_pk_max_f16 v182, v182, 0
	v_pk_max_f16 v183, v183, 0
	s_waitcnt lgkmcnt(1)
	v_mfma_f32_16x16x32_f16 v[252:255], v[240:243], v[232:235], 0
	v_cvt_pk_f16_f32 v232, v172, v173
	v_cvt_pk_f16_f32 v233, v174, v175
	v_pk_max_f16 v232, v232, 0
	v_pk_max_f16 v233, v233, 0
	v_mfma_f32_16x16x32_f16 v[184:187], v[176:179], v[196:199], v[184:187]
	v_cvt_pk_f16_f32 v188, v212, v213
	v_cvt_pk_f16_f32 v189, v214, v215
	v_pk_max_f16 v188, v188, 0
	v_pk_max_f16 v189, v189, 0
	s_waitcnt lgkmcnt(0)
	v_mfma_f32_16x16x32_f16 v[252:255], v[244:247], v[236:239], v[252:255]
	ds_read_u16 v102, v114
	ds_read_u16 v103, v114 offset:512
	ds_read_u16 v115, v114 offset:1024
	ds_read_u16 v116, v114 offset:1536
	v_cvt_pk_f16_f32 v234, v224, v225
	v_cvt_pk_f16_f32 v235, v226, v227
	v_pk_max_f16 v234, v234, 0
	v_pk_max_f16 v235, v235, 0
	v_mfma_f32_16x16x32_f16 v[160:163], v[220:223], v[196:199], v[160:163]
	v_cvt_pk_f16_f32 v190, v204, v205
	v_cvt_pk_f16_f32 v191, v206, v207
	v_pk_max_f16 v190, v190, 0
	v_pk_max_f16 v191, v191, 0
	v_mfma_f32_16x16x32_f16 v[192:195], v[240:243], v[180:183], 0
	v_cvt_pk_f16_f32 v236, v228, v229
	v_cvt_pk_f16_f32 v237, v230, v231
	v_pk_max_f16 v236, v236, 0
	v_pk_max_f16 v237, v237, 0
	v_mfma_f32_16x16x32_f16 v[192:195], v[244:247], v[188:191], v[192:195]
	v_cvt_pk_f16_f32 v238, v216, v217
	v_cvt_pk_f16_f32 v239, v218, v219
	v_pk_max_f16 v238, v238, 0
	v_pk_max_f16 v239, v239, 0
	v_cvt_pk_f16_f32 v180, v200, v201
	v_cvt_pk_f16_f32 v181, v202, v203
	v_pk_max_f16 v180, v180, 0
	v_pk_max_f16 v181, v181, 0
	v_mfma_f32_16x16x32_f16 v[196:199], v[240:243], v[232:235], 0
	v_cvt_pk_f16_f32 v182, v136, v137
	v_cvt_pk_f16_f32 v183, v138, v139
	v_pk_max_f16 v182, v182, 0
	v_pk_max_f16 v183, v183, 0
	v_mfma_f32_16x16x32_f16 v[196:199], v[244:247], v[236:239], v[196:199]
	v_cvt_pk_f16_f32 v188, v184, v185
	v_cvt_pk_f16_f32 v189, v186, v187
	v_pk_max_f16 v188, v188, 0
	v_pk_max_f16 v189, v189, 0
	v_cvt_pk_f16_f32 v190, v160, v161
	v_cvt_pk_f16_f32 v191, v162, v163
	v_pk_max_f16 v190, v190, 0
	v_pk_max_f16 v191, v191, 0
	v_mfma_f32_16x16x32_f16 v[122:125], v[240:243], v[180:183], 0
	s_nop 0
	v_mfma_f32_16x16x32_f16 v[122:125], v[244:247], v[188:191], v[122:125]
	v_add_u32_e32 v145, 0x12c00, v105
	v_cndmask_b32_e64 v0, v252, v192, s[2:3]
	v_cndmask_b32_e64 v0, v0, v196, s[0:1]
	s_waitcnt vmcnt(16)
	v_cndmask_b32_e64 v1, v30, v134, s[0:1]
	v_bfi_b32 v30, s10, v1, v30
	v_perm_b32 v1, v22, v134, s24
	v_cndmask_b32_e64 v22, v22, v1, s[0:1]
	v_cndmask_b32_e64 v0, v0, v122, s[26:27]
	ds_write_b32 v112, v0
	v_bfi_b32 v1, s10, v135, v18
	v_perm_b32 v121, v10, v135, s24
	v_cndmask_b32_e64 v18, v18, v1, s[0:1]
	v_cndmask_b32_e64 v10, v10, v121, s[0:1]
	s_add_i32 s22, s22, 0x80000
	s_add_i32 s11, s11, 1
	s_add_u32 s12, s12, 4
	s_addc_u32 s13, s13, 0
	v_add_u32_e32 v104, 0x400, v104
	v_add_u32_e32 v105, 0x800, v105
	v_add_u32_e32 v114, 2, v114
	s_cmp_eq_u32 s22, 0x898000
	s_waitcnt lgkmcnt(0)
	s_barrier
	ds_read_b128 v[232:235], v113
	ds_read_b128 v[236:239], v113 offset:1024
	ds_read_b128 v[240:243], v145 offset:2048
	ds_read_b128 v[244:247], v145 offset:2064
	ds_read_b128 v[248:251], v145 offset:2080
	ds_read_b128 v[252:255], v145 offset:2096
	s_waitcnt lgkmcnt(4)
	v_add_f32_e32 v0, v232, v233
	v_add_f32_e32 v1, v234, v235
	v_add_f32_e32 v121, v236, v237
	v_add_f32_e32 v144, v238, v239
	v_add_f32_e32 v0, v0, v1
	v_add_f32_e32 v121, v121, v144
	v_add_f32_e32 v0, v0, v121
	v_add_f32_e32 v0, s30, v0
	v_cvt_f16_f32_e32 v1, v0
	v_cvt_f16_f32_e32 v121, v0
	ds_write_b32 v106, v0
	v_add_u32_e32 v106, 4, v106
	v_permlane16_swap_b32_e32 v1, v121
	s_cbranch_scc0 .LBB1_4
